# XCD-contiguous MoE order + phase 5: chain workgroups no longer run an attention unit behind their scan; the builder workgroups take all 2048 attention units (post-scan attention block deleted)
# baseline (speedup 1.0000x reference)
.LBB0_6:
	s_ashr_i32 s3, s2, 31
	s_lshr_b32 s0, s3, 29
	s_add_i32 s5, s2, s0
	s_and_b32 s0, s5, -8
	s_sub_i32 s18, s2, s0
	s_lshl_b32 s0, s18, 4
	s_cmp_lt_i32 s18, 0
	s_mul_i32 s1, s18, 17
	s_cselect_b32 s0, s1, s0
	s_lshl_b32 s1, s18, 7
	s_cmp_lt_i32 s18, 0
	s_mul_i32 s4, s18, 0x81
	s_cselect_b32 s1, s4, s1
	s_lshl_b32 s4, s18, 6
	s_cmp_lt_i32 s18, 0
	s_movk_i32 s6, 0xc1
	s_mul_i32 s7, s18, 0x41
	s_movk_i32 s9, 0x181
	s_cselect_b32 s6, s6, 0xc0
	s_cselect_b32 s9, s9, 0x180
	s_cselect_b32 s4, s7, s4
	s_lshl_b32 s11, s2, 3
	s_lshl_b32 s7, s2, 9
	s_cmp_eq_u32 s8, 15
	v_writelane_b32 v253, s7, 6
	s_cselect_b64 s[12:13], -1, 0
	v_writelane_b32 v253, s12, 7
	s_cmp_eq_u32 s8, 14
	v_mov_b32_e32 v35, 0
	v_writelane_b32 v253, s13, 8
	s_cselect_b64 s[12:13], -1, 0
	v_writelane_b32 v253, s12, 9
	s_cmp_eq_u32 s8, 13
	s_mov_b32 s59, 0x20000
	v_writelane_b32 v253, s13, 10
	s_cselect_b64 s[12:13], -1, 0
	v_writelane_b32 v253, s12, 11
	s_cmp_eq_u32 s8, 12
	v_mbcnt_lo_u32_b32 v1, -1, 0
	v_writelane_b32 v253, s13, 12
	s_cselect_b64 s[12:13], -1, 0
	v_writelane_b32 v253, s12, 13
	s_cmp_eq_u32 s8, 11
	v_mov_b32_e32 v214, 0x358637bd
	v_writelane_b32 v253, s13, 14
	s_cselect_b64 s[12:13], -1, 0
	v_writelane_b32 v253, s12, 15
	s_cmp_eq_u32 s8, 10
	v_mov_b32_e32 v215, 1
	v_writelane_b32 v253, s13, 16
	s_cselect_b64 s[12:13], -1, 0
	v_writelane_b32 v253, s12, 17
	s_cmp_eq_u32 s8, 9
	s_movk_i32 s66, 0x4800
	v_writelane_b32 v253, s13, 18
	s_cselect_b64 s[12:13], -1, 0
	v_writelane_b32 v253, s12, 19
	s_cmp_eq_u32 s8, 8
	s_mov_b32 s67, s59
	v_writelane_b32 v253, s13, 20
	s_cselect_b64 s[12:13], -1, 0
	v_writelane_b32 v253, s12, 21
	s_cmp_eq_u32 s8, 7
	s_mov_b32 s58, 0x4f700000
	v_writelane_b32 v253, s13, 22
	s_cselect_b64 s[12:13], -1, 0
	v_writelane_b32 v253, s12, 23
	s_cmp_eq_u32 s8, 6
	v_mov_b32_e32 v216, 0x3a27c5ac
	v_writelane_b32 v253, s13, 24
	s_cselect_b64 s[12:13], -1, 0
	v_writelane_b32 v253, s12, 25
	s_cmp_eq_u32 s8, 5
	v_mov_b32_e32 v234, v35
	v_writelane_b32 v253, s13, 26
	s_cselect_b64 s[12:13], -1, 0
	v_writelane_b32 v253, s12, 27
	s_cmp_eq_u32 s8, 4
	v_mov_b32_e32 v235, v35
	v_writelane_b32 v253, s13, 28
	s_cselect_b64 s[12:13], -1, 0
	v_writelane_b32 v253, s12, 29
	s_cmp_eq_u32 s8, 3
	v_mov_b32_e32 v236, v35
	v_writelane_b32 v253, s13, 30
	s_cselect_b64 s[12:13], -1, 0
	v_writelane_b32 v253, s12, 31
	s_cmp_eq_u32 s8, 2
	v_mov_b32_e32 v237, v35
	v_writelane_b32 v253, s13, 32
	s_cselect_b64 s[12:13], -1, 0
	v_writelane_b32 v253, s12, 33
	s_cmp_eq_u32 s8, 1
	v_mov_b32_e32 v217, 2
	v_writelane_b32 v253, s13, 34
	s_cselect_b64 s[12:13], -1, 0
	v_writelane_b32 v253, s12, 35
	s_cmp_eq_u32 s8, 0
	v_mbcnt_hi_u32_b32 v218, -1, v1
	v_writelane_b32 v253, s13, 36
	s_cselect_b64 s[12:13], -1, 0
	v_writelane_b32 v253, s12, 37
	s_lshl_b32 s7, s8, 6
	s_cmpk_lt_i32 s2, 0xc00
	v_writelane_b32 v253, s13, 38
	v_writelane_b32 v253, s7, 39
	s_cselect_b64 s[12:13], -1, 0
	s_ashr_i32 s8, s5, 3
	v_writelane_b32 v253, s12, 40
	s_cmpk_lt_i32 s2, 0x600
	s_mul_i32 s5, s6, s18
	v_writelane_b32 v253, s13, 41
	s_cselect_b64 s[12:13], -1, 0
	s_add_i32 s5, s5, s8
	s_mul_hi_i32 s6, s5, 0x2aaaaaab
	s_lshr_b32 s7, s6, 31
	s_ashr_i32 s6, s6, 3
	s_add_i32 s6, s6, s7
	s_mul_i32 s7, s6, 48
	s_sub_i32 s5, s5, s7
	s_bfe_i32 s7, s5, 0x80000
	s_bfe_u32 s7, s7, 0x2000d
	s_add_i32 s7, s5, s7
	s_bfe_i32 s10, s7, 0x80000
	s_and_b32 s7, s7, 0xfc
	s_sub_i32 s5, s5, s7
	s_lshl_b32 s6, s6, 2
	s_sext_i32_i8 s5, s5
	v_writelane_b32 v253, s12, 42
	s_add_i32 s14, s6, s5
	s_mov_b32 s6, s14
	v_writelane_b32 v253, s13, 43
	s_ashr_i32 s15, s14, 31
	v_writelane_b32 v253, s6, 44
	s_sext_i32_i16 s10, s10
	s_ashr_i32 s16, s10, 4
	v_writelane_b32 v253, s7, 45
	s_lshl_b64 s[6:7], s[14:15], 19
	v_writelane_b32 v253, s6, 46
	s_lshl_b32 s5, s16, 9
	s_ashr_i32 s17, s16, 31
	v_writelane_b32 v253, s7, 47
	v_writelane_b32 v253, s5, 48
	s_ashr_i32 s5, s5, 31
	v_writelane_b32 v253, s5, 49
	s_mov_b32 s6, s16
	v_writelane_b32 v253, s6, 50
	s_ashr_i32 s12, s10, 2
	s_lshl_b32 s5, s12, 17
	v_writelane_b32 v253, s7, 51
	s_lshl_b64 s[6:7], s[16:17], 19
	v_writelane_b32 v253, s6, 52
	s_and_b32 s5, s5, 0x60000
	s_cmpk_lt_i32 s2, 0x200
	v_writelane_b32 v253, s7, 53
	v_writelane_b32 v253, s12, 54
	v_writelane_b32 v253, s5, 55
	s_cselect_b64 s[6:7], -1, 0
	v_writelane_b32 v253, s6, 56
	s_cmp_lt_i32 s2, 32
	v_mov_b64_e32 v[200:201], 0xc00
	v_writelane_b32 v253, s7, 57
	s_cselect_b64 s[6:7], -1, 0
	s_cmp_gt_i32 s2, 31
	v_writelane_b32 v253, s6, 58
	s_cselect_b64 s[12:13], -1, 0
	v_mov_b64_e32 v[202:203], 0xbff
	v_writelane_b32 v253, s7, 59
	s_and_b64 s[6:7], s[12:13], exec
	s_cselect_b32 s5, s2, 0x820
	s_sub_i32 s5, s5, 32
	s_bitcmp1_b32 s2, 3
	s_cselect_b64 s[6:7], -1, 0
	v_writelane_b32 v253, s12, 60
	s_and_b64 s[94:95], s[12:13], s[6:7]
	s_cmpk_lt_i32 s11, 0x4000
	v_writelane_b32 v253, s13, 61
	s_cselect_b64 s[6:7], -1, 0
	s_cmpk_lt_u32 s5, 0x800
	v_writelane_b32 v253, s11, 62
	s_cselect_b64 s[10:11], -1, 0
	s_or_b64 s[6:7], s[6:7], s[10:11]
	v_writelane_b32 v253, s5, 63
	v_writelane_b32 v254, s6, 0
	s_mul_i32 s5, s2, 0x120000
	s_lshl_b32 s80, s2, 6
	v_writelane_b32 v254, s7, 1
	s_add_i32 s6, s5, 0x3c800000
	v_writelane_b32 v254, s6, 2
	s_add_i32 s6, s5, 0x3c804800
	v_writelane_b32 v254, s6, 3
	s_add_i32 s6, s5, 0x3c809000
	v_writelane_b32 v254, s6, 4
	s_add_i32 s6, s5, 0x3c80d800
	v_writelane_b32 v254, s6, 5
	s_add_i32 s6, s5, 0x3c812000
	v_writelane_b32 v254, s6, 6
	s_add_i32 s6, s5, 0x3c816800
	v_writelane_b32 v254, s6, 7
	s_add_i32 s6, s5, 0x3c81b000
	v_writelane_b32 v254, s6, 8
	s_add_i32 s6, s5, 0x3c81f800
	v_writelane_b32 v254, s6, 9
	s_add_i32 s6, s5, 0x3c824000
	v_writelane_b32 v254, s6, 10
	s_add_i32 s5, s5, 0x3c828800
	v_writelane_b32 v254, s5, 11
	s_lshl_b32 s5, s2, 21
	s_add_i32 s6, s5, 0x307fc800
	v_writelane_b32 v254, s6, 12
	s_add_i32 s6, s5, 0x307fd800
	v_writelane_b32 v254, s6, 13
	s_add_i32 s6, s5, 0x307fe800
	v_writelane_b32 v254, s6, 14
	s_add_i32 s6, s5, 0x307ff800
	v_writelane_b32 v254, s6, 15
	s_add_i32 s6, s5, 0x30800800
	v_writelane_b32 v254, s6, 16
	s_add_i32 s6, s5, 0x30801800
	v_writelane_b32 v254, s6, 17
	s_add_i32 s6, s5, 0x30802800
	v_writelane_b32 v254, s6, 18
	s_add_i32 s6, s5, 0x30803800
	s_add_i32 s82, s5, 0x307fb800
	v_writelane_b32 v254, s6, 19
	s_add_i32 s5, s5, 0x30804800
	s_ashr_i32 s81, s80, 31
	v_writelane_b32 v254, s5, 20
	s_lshl_b64 s[6:7], s[2:3], 18
	v_writelane_b32 v254, s6, 21
	s_cmpk_lt_i32 s2, 0x400
	s_mul_i32 s5, s18, s9
	v_writelane_b32 v254, s7, 22
	s_cselect_b64 s[6:7], -1, 0
	s_bfe_u32 s19, s2, 0x10003
	v_writelane_b32 v254, s6, 23
	s_cmpk_lt_i32 s2, 0x80
	v_not_b32_e32 v219, 63
	v_writelane_b32 v254, s7, 24
	s_cselect_b64 s[6:7], -1, 0
	v_writelane_b32 v254, s6, 25
	s_cmpk_gt_i32 s2, 0x7f
	v_not_b32_e32 v220, 31
	v_writelane_b32 v254, s7, 26
	s_cselect_b64 s[6:7], -1, 0
	s_cmpk_lt_i32 s2, 0x100
	s_cselect_b64 s[10:11], -1, 0
	s_add_i32 s5, s5, s8
	v_writelane_b32 v254, s10, 27
	s_mul_hi_i32 s9, s5, 0x2aaaaaab
	s_add_i32 s4, s4, s8
	v_writelane_b32 v254, s11, 28
	s_lshr_b32 s10, s9, 31
	s_ashr_i32 s9, s9, 4
	s_add_i32 s10, s9, s10
	s_mul_i32 s9, s10, 0x60
	s_sub_i32 s5, s5, s9
	s_bfe_i32 s9, s5, 0x80000
	s_bfe_u32 s9, s9, 0x2000d
	s_add_i32 s11, s5, s9
	s_and_b32 s9, s11, 0xfc
	s_sub_i32 s5, s5, s9
	s_ashr_i32 s9, s4, 31
	s_lshr_b32 s9, s9, 28
	s_add_i32 s12, s4, s9
	s_and_b32 s9, s12, 0xfff0
	s_sub_i32 s4, s4, s9
	s_bfe_i32 s9, s4, 0x80000
	s_bfe_u32 s9, s9, 0x2000d
	s_add_i32 s13, s4, s9
	s_and_b32 s9, s13, 0xfc
	s_add_i32 s1, s1, s8
	s_sub_i32 s4, s4, s9
	s_ashr_i32 s9, s1, 31
	s_lshr_b32 s9, s9, 27
	s_add_i32 s14, s1, s9
	s_and_b32 s9, s14, 0xffe0
	s_sub_i32 s1, s1, s9
	s_bfe_i32 s9, s1, 0x80000
	s_bfe_u32 s9, s9, 0x2000d
	s_add_i32 s15, s1, s9
	s_and_b32 s9, s15, 0xfc
	s_sub_i32 s16, s1, s9
	s_lshr_b32 s1, s3, 30
	s_add_i32 s1, s2, s1
	s_ashr_i32 s9, s1, 2
	v_writelane_b32 v254, s9, 29
	s_add_i32 s9, 0, 0x20000
	s_lshl_b32 s17, s8, 2
	s_and_b32 s1, s1, -4
	s_add_i32 s17, s9, s17
	v_writelane_b32 v254, s17, 30
	s_add_i32 s9, s9, s1
	v_writelane_b32 v254, s9, 31
	s_ashr_i32 s9, s8, 31
	s_sub_i32 s24, s2, s1
	s_add_i32 s26, s0, s8
	s_lshl_b64 s[0:1], s[8:9], 18
	v_writelane_b32 v254, s0, 32
	s_sext_i32_i8 s5, s5
	s_sext_i32_i8 s4, s4
	v_writelane_b32 v254, s1, 33
	s_bfe_i32 s1, s11, 0x80000
	s_lshl_b32 s0, s10, 2
	s_sext_i32_i16 s1, s1
	s_add_i32 s20, s0, s5
	s_ashr_i32 s0, s1, 2
	v_writelane_b32 v254, s0, 34
	s_lshr_b32 s0, s1, 2
	s_bfe_i64 s[0:1], s[0:1], 0x100000
	s_lshl_b64 s[0:1], s[0:1], 20
	v_writelane_b32 v254, s0, 35
	s_ashr_i32 s25, s24, 31
	s_mov_b32 s8, s19
	v_writelane_b32 v254, s1, 36
	s_ashr_i32 s0, s12, 4
	s_bfe_i32 s1, s13, 0x80000
	s_lshl_b32 s0, s0, 2
	s_sext_i32_i16 s1, s1
	s_add_i32 s22, s0, s4
	s_lshr_b32 s0, s1, 2
	s_ashr_i32 s5, s1, 2
	s_bfe_i64 s[0:1], s[0:1], 0x100000
	s_lshl_b64 s[0:1], s[0:1], 17
	v_writelane_b32 v254, s0, 37
	s_sext_i32_i8 s4, s16
	s_ashr_i32 s19, s18, 31
	v_writelane_b32 v254, s1, 38
	s_ashr_i32 s0, s14, 5
	s_bfe_i32 s1, s15, 0x80000
	s_lshl_b32 s0, s0, 2
	s_sext_i32_i16 s1, s1
	s_add_i32 s88, s0, s4
	s_lshr_b32 s0, s1, 2
	s_ashr_i32 s83, s1, 2
	s_bfe_i64 s[0:1], s[0:1], 0x100000
	s_lshl_b64 s[14:15], s[0:1], 19
	v_writelane_b32 v254, s14, 39
	s_lshl_b64 s[0:1], s[0:1], 20
	s_ashr_i32 s21, s20, 31
	v_writelane_b32 v254, s15, 40
	v_writelane_b32 v254, s0, 41
	s_ashr_i32 s23, s22, 31
	s_ashr_i32 s89, s88, 31
	v_writelane_b32 v254, s1, 42
	v_writelane_b32 v254, s5, 43
	s_lshl_b32 s0, s5, 9
	v_writelane_b32 v254, s0, 44
	s_ashr_i32 s0, s0, 31
	v_writelane_b32 v254, s0, 45
	s_mov_b32 s0, s24
	v_writelane_b32 v254, s0, 46
	s_ashr_i32 s27, s26, 31
	v_mov_b32_e32 v221, 0x7fc00000
	v_writelane_b32 v254, s1, 47
	s_lshl_b64 s[0:1], s[24:25], 20
	v_writelane_b32 v254, s0, 48
	v_mov_b32_e32 v222, 0x80
	v_mov_b32_e32 v223, 0xff800000
	v_writelane_b32 v254, s1, 49
	s_mov_b32 s0, s18
	v_writelane_b32 v254, s0, 50
	v_mov_b64_e32 v[204:205], 0x400
	v_mov_b64_e32 v[206:207], 0x3ff
	v_writelane_b32 v254, s1, 51
	s_lshl_b64 s[0:1], s[18:19], 18
	v_writelane_b32 v254, s0, 52
	v_mov_b64_e32 v[210:211], 0x7f
	s_movk_i32 s33, 0xc0
	v_writelane_b32 v254, s1, 53
	s_lshr_b32 s97, s93, 3
	s_and_b32 s96, s2, 7
	s_mul_i32 s96, s96, s97
	s_lshr_b32 s97, s2, 3
	s_add_i32 s96, s96, s97
	s_and_b32 s97, s93, 7
	s_cmp_eq_u32 s97, 0
	s_cselect_b32 s96, s96, s2
	v_writelane_b32 v252, s96, 47
	s_lshr_b32 s97, s96, 2
	v_writelane_b32 v254, s97, 29
	s_and_b32 s97, s96, -4
	s_add_i32 s97, s97, 0x20000
	v_writelane_b32 v254, s97, 31
	s_and_b32 s97, s96, 3
	v_writelane_b32 v254, s97, 46
	s_lshl_b32 s97, s97, 20
	v_writelane_b32 v254, s97, 48
	s_lshr_b32 s97, s96, 3
	s_lshl_b32 s97, s97, 2
	s_add_i32 s97, s97, 0x20000
	v_writelane_b32 v254, s97, 30
	s_lshr_b32 s97, s96, 3
	s_lshl_b32 s97, s97, 18
	v_writelane_b32 v254, s97, 32
	s_and_b32 s97, s96, 7
	v_writelane_b32 v254, s97, 50
	s_lshl_b32 s97, s97, 18
	v_writelane_b32 v254, s97, 52
	s_mov_b32 s97, 0
	v_writelane_b32 v254, s97, 47
	v_writelane_b32 v254, s97, 49
	v_writelane_b32 v254, s97, 51
	v_writelane_b32 v254, s97, 53
	v_writelane_b32 v254, s97, 33
	s_mov_b32 s0, s20
	v_writelane_b32 v254, s0, 54
	s_movk_i32 s72, 0x7fff
	s_movk_i32 s73, 0x1000
	v_writelane_b32 v254, s1, 55
	s_lshl_b64 s[0:1], s[20:21], 20
	v_writelane_b32 v254, s0, 56
	s_movk_i32 s90, 0x2000
	s_movk_i32 s91, 0x3000
	v_writelane_b32 v254, s1, 57
	s_mov_b32 s0, s22
	v_writelane_b32 v254, s0, 58
	s_mov_b32 s92, 0x34800000
	s_mov_b32 s97, 0
	v_writelane_b32 v254, s1, 59
	s_lshl_b64 s[0:1], s[22:23], 19
	v_writelane_b32 v254, s0, 60
	s_mov_b64 s[78:79], 0x80
	s_mov_b64 s[76:77], 0x8000000
	v_writelane_b32 v254, s1, 61
	s_lshl_b64 s[0:1], s[88:89], 19
	v_writelane_b32 v254, s0, 62
	s_nop 1
	v_writelane_b32 v254, s1, 63
	s_lshl_b64 s[0:1], s[88:89], 20
	v_writelane_b32 v252, s0, 0
	s_nop 1
	v_writelane_b32 v252, s1, 1
	s_mov_b32 s0, s26
	v_writelane_b32 v252, s0, 2
	s_nop 1
	v_writelane_b32 v252, s1, 3
	s_lshl_b64 s[0:1], s[26:27], 20
	v_writelane_b32 v252, s0, 4
	s_nop 1
	v_writelane_b32 v252, s1, 5
	s_xor_b64 s[0:1], s[94:95], -1
	v_writelane_b32 v252, s0, 6
	s_nop 1
	v_writelane_b32 v252, s1, 7
	s_add_u32 s0, s60, 0x1000
	v_writelane_b32 v252, s0, 8
	s_addc_u32 s0, s61, 0
	v_writelane_b32 v252, s0, 9
	s_xor_b64 s[0:1], s[6:7], -1
	v_writelane_b32 v252, s0, 10
	s_add_i32 s4, 0, 0x20600
	s_mov_b32 s6, 0x3ffff
	v_writelane_b32 v252, s1, 11
	s_lshl_b32 s0, s2, 4
	v_writelane_b32 v252, s0, 12
	s_lshl_b32 s0, s2, 7
	v_writelane_b32 v252, s0, 13
	s_or_b32 s0, s0, 1
	v_writelane_b32 v252, s0, 14
	s_lshl_b32 s0, s2, 5
	v_writelane_b32 v252, s0, 15
	s_lshl_b32 s0, s2, 8
	v_writelane_b32 v252, s0, 16
	s_add_i32 s0, 0, 0x24020
	v_writelane_b32 v252, s0, 17
	s_add_i32 s0, 0, 0x24024
	v_writelane_b32 v252, s0, 18
	v_writelane_b32 v252, s4, 19
	s_add_i32 s4, 0, 0x20800
	v_writelane_b32 v252, s4, 20
	s_add_i32 s4, 0, 0x20a00
	v_writelane_b32 v252, s4, 21
	s_lshl_b64 s[4:5], s[80:81], 2
	v_writelane_b32 v252, s4, 22
	s_mov_b32 s0, 0x24800000
	s_mov_b32 s1, 0x2c800000
	v_writelane_b32 v252, s5, 23
	s_load_dwordx2 s[4:5], s[84:85], 0x100
	v_writelane_b32 v252, s84, 24
	s_waitcnt lgkmcnt(0)
	s_mov_b32 s48, s4
	v_writelane_b32 v252, s85, 25
	v_writelane_b32 v252, s93, 26
	v_writelane_b32 v252, s86, 27
	s_nop 1
	v_writelane_b32 v252, s87, 28
	v_writelane_b32 v252, s80, 29
	s_nop 1
	v_writelane_b32 v252, s81, 30
	v_writelane_b32 v252, s82, 31
	v_writelane_b32 v252, s88, 32
	s_nop 1
	v_writelane_b32 v252, s89, 33
	v_writelane_b32 v252, s83, 34
	s_branch .LBB0_8

.LBB0_504:
	s_waitcnt vmcnt(0)
	v_mov_b32_e32 v2, v0
	s_mov_b32 s4, s93
	v_readlane_b32 s48, v252, 35
	v_readfirstlane_b32 s20, v2
	s_mov_b64 s[4:5], s[62:63]
	s_mov_b32 s14, 19
	s_and_b64 vcc, exec, s[22:23]
	v_readlane_b32 s49, v252, 36
.LBB0_507:
	s_waitcnt vmcnt(0)
	s_waitcnt lgkmcnt(0)
	s_barrier
	s_mov_b64 s[18:19], exec
	v_readlane_b32 s4, v253, 2
	v_readlane_b32 s5, v253, 3
	s_and_b64 s[4:5], s[18:19], s[4:5]
	s_mov_b64 exec, s[4:5]
	s_cbranch_execz .LBB0_551
	v_readlane_b32 s4, v252, 17
	s_mov_b64 s[20:21], s[86:87]
	s_waitcnt vmcnt(0) expcnt(0) lgkmcnt(0)
	v_mov_b32_e32 v1, s4
	ds_read_b32 v4, v1
	v_readlane_b32 s4, v252, 18
	s_waitcnt lgkmcnt(0)
	v_cmp_ne_u32_e32 vcc, 0, v4
	v_mov_b32_e32 v1, s4
	ds_read_b32 v2, v1
	s_cbranch_vccnz .LBB0_522
	v_readlane_b32 s14, v253, 0
	v_readlane_b32 s15, v253, 1
	s_add_u32 s22, s20, 0x1000
	s_load_dwordx2 s[4:5], s[14:15], 0x4
	s_addc_u32 s23, s21, 0
	s_add_u32 s24, s20, 0x1100
	s_addc_u32 s25, s21, 0
	s_add_u32 s26, s20, 0x1200
	s_addc_u32 s27, s21, 0
	s_waitcnt lgkmcnt(0)
	s_mul_i32 s16, s4, s93
	s_add_u32 s28, s20, 0x1300
	s_mul_i32 s16, s16, s5
	s_addc_u32 s29, s21, 0
	s_mov_b32 s17, 1
	s_mov_b64 s[30:31], 0
	s_branch .LBB0_512
